# baseline (speedup 1.0000x reference)
.LBB2_3:
	s_mul_i32 s15, s14, 0xe000
	s_add_i32 s14, s14, 1
	s_cmp_lg_u32 s14, 2
	s_cselect_b32 s14, s14, 0
	s_add_i32 s20, s15, s21
	v_add3_u32 v206, s15, v147, v148
	v_add3_u32 v207, s15, v146, v148
	s_waitcnt lgkmcnt(8)
	v_mfma_f32_16x16x32_f16 v[134:137], v[98:101], v[118:121], v[134:137]
	s_waitcnt lgkmcnt(7)
	v_mfma_f32_16x16x32_f16 v[130:133], v[90:93], v[118:121], v[130:133]
	s_waitcnt lgkmcnt(6)
	v_mfma_f32_16x16x32_f16 v[102:105], v[98:101], v[106:109], v[102:105]
	ds_read_b128 v[152:155], v206
	v_mfma_f32_16x16x32_f16 v[94:97], v[90:93], v[106:109], v[94:97]
	ds_read_b128 v[168:171], v207 offset:32768
	s_waitcnt lgkmcnt(7)
	v_mfma_f32_16x16x32_f16 v[126:129], v[82:85], v[118:121], v[126:129]
	ds_read_b128 v[172:175], v207 offset:34816
	v_mfma_f32_16x16x32_f16 v[78:81], v[82:85], v[106:109], v[78:81]
	ds_read_b128 v[156:159], v206 offset:2048
	s_waitcnt lgkmcnt(8)
	v_mfma_f32_16x16x32_f16 v[122:125], v[74:77], v[118:121], v[122:125]
	ds_read_b128 v[176:179], v207 offset:36864
	v_mfma_f32_16x16x32_f16 v[70:73], v[74:77], v[106:109], v[70:73]
	ds_read_b128 v[180:183], v207 offset:38912
	s_waitcnt lgkmcnt(9)
	v_mfma_f32_16x16x32_f16 v[54:57], v[98:101], v[86:89], v[54:57]
	ds_read_b128 v[160:163], v206 offset:4096
	v_mfma_f32_16x16x32_f16 v[46:49], v[90:93], v[86:89], v[46:49]
	ds_read_b128 v[184:187], v207 offset:40960
	v_mfma_f32_16x16x32_f16 v[42:45], v[82:85], v[86:89], v[42:45]
	ds_read_b128 v[188:191], v207 offset:43008
	v_mfma_f32_16x16x32_f16 v[38:41], v[74:77], v[86:89], v[38:41]
	ds_read_b128 v[164:167], v206 offset:6144
	s_waitcnt lgkmcnt(12)
	v_mfma_f32_16x16x32_f16 v[114:117], v[66:69], v[118:121], v[114:117]
	v_mfma_f32_16x16x32_f16 v[62:65], v[66:69], v[106:109], v[62:65]
	v_mfma_f32_16x16x32_f16 v[30:33], v[66:69], v[86:89], v[30:33]
	s_waitcnt lgkmcnt(11)
	v_mfma_f32_16x16x32_f16 v[110:113], v[50:53], v[118:121], v[110:113]
	v_mfma_f32_16x16x32_f16 v[58:61], v[50:53], v[106:109], v[58:61]
	v_mfma_f32_16x16x32_f16 v[26:29], v[50:53], v[86:89], v[26:29]
	s_waitcnt lgkmcnt(10)
	v_mfma_f32_16x16x32_f16 v[22:25], v[98:101], v[34:37], v[22:25]
	v_mfma_f32_16x16x32_f16 v[18:21], v[90:93], v[34:37], v[18:21]
	v_mfma_f32_16x16x32_f16 v[14:17], v[82:85], v[34:37], v[14:17]
	v_mfma_f32_16x16x32_f16 v[10:13], v[74:77], v[34:37], v[10:13]
	v_mfma_f32_16x16x32_f16 v[6:9], v[66:69], v[34:37], v[6:9]
	v_mfma_f32_16x16x32_f16 v[2:5], v[50:53], v[34:37], v[2:5]
	s_waitcnt vmcnt(0) lgkmcnt(0)
	s_barrier
	s_mov_b32 m0, s20
	s_mul_i32 s15, s14, 0xe000
	v_mfma_f32_16x16x32_f16 v[134:137], v[168:171], v[152:155], v[134:137]
	v_add_u32_e32 v206, s15, v150
	v_add_u32_e32 v207, s15, v151
	v_mfma_f32_16x16x32_f16 v[130:133], v[172:175], v[152:155], v[130:133]
	ds_read_b128 v[118:121], v206
	v_mfma_f32_16x16x32_f16 v[126:129], v[176:179], v[152:155], v[126:129]
	ds_read_b128 v[98:101], v207 offset:32768
	v_mfma_f32_16x16x32_f16 v[122:125], v[180:183], v[152:155], v[122:125]
	ds_read_b128 v[90:93], v207 offset:34816
	v_mfma_f32_16x16x32_f16 v[114:117], v[184:187], v[152:155], v[114:117]
	ds_read_b128 v[106:109], v206 offset:2048
	v_mfma_f32_16x16x32_f16 v[110:113], v[188:191], v[152:155], v[110:113]
	ds_read_b128 v[82:85], v207 offset:36864
	v_mfma_f32_16x16x32_f16 v[102:105], v[168:171], v[156:159], v[102:105]
	ds_read_b128 v[74:77], v207 offset:38912
	v_mfma_f32_16x16x32_f16 v[94:97], v[172:175], v[156:159], v[94:97]
	ds_read_b128 v[86:89], v206 offset:4096
	v_mfma_f32_16x16x32_f16 v[78:81], v[176:179], v[156:159], v[78:81]
	ds_read_b128 v[66:69], v207 offset:40960
	v_mfma_f32_16x16x32_f16 v[70:73], v[180:183], v[156:159], v[70:73]
	ds_read_b128 v[50:53], v207 offset:43008
	v_mfma_f32_16x16x32_f16 v[62:65], v[184:187], v[156:159], v[62:65]
	ds_read_b128 v[34:37], v206 offset:6144
	v_mfma_f32_16x16x32_f16 v[58:61], v[188:191], v[156:159], v[58:61]
	global_load_lds_dwordx4 v[192:193], off
	v_lshl_add_u64 v[192:193], v[192:193], 0, s[22:23]
	s_add_u32 m0, s20, 0x2000
	v_mfma_f32_16x16x32_f16 v[54:57], v[168:171], v[160:163], v[54:57]
	v_mfma_f32_16x16x32_f16 v[46:49], v[172:175], v[160:163], v[46:49]
	global_load_lds_dwordx4 v[194:195], off
	v_lshl_add_u64 v[194:195], v[194:195], 0, s[22:23]
	s_add_u32 m0, s20, 0x4000
	v_mfma_f32_16x16x32_f16 v[42:45], v[176:179], v[160:163], v[42:45]
	v_mfma_f32_16x16x32_f16 v[38:41], v[180:183], v[160:163], v[38:41]
	global_load_lds_dwordx4 v[196:197], off
	v_lshl_add_u64 v[196:197], v[196:197], 0, s[22:23]
	s_add_u32 m0, s20, 0x6000
	v_mfma_f32_16x16x32_f16 v[30:33], v[184:187], v[160:163], v[30:33]
	v_mfma_f32_16x16x32_f16 v[26:29], v[188:191], v[160:163], v[26:29]
	global_load_lds_dwordx4 v[198:199], off
	v_lshl_add_u64 v[198:199], v[198:199], 0, s[22:23]
	s_add_u32 m0, s20, 0x8000
	v_mfma_f32_16x16x32_f16 v[22:25], v[168:171], v[164:167], v[22:25]
	v_mfma_f32_16x16x32_f16 v[18:21], v[172:175], v[164:167], v[18:21]
	global_load_lds_dwordx4 v[200:201], off
	v_lshl_add_u64 v[200:201], v[200:201], 0, s[22:23]
	s_add_u32 m0, s20, 0xa000
	v_mfma_f32_16x16x32_f16 v[14:17], v[176:179], v[164:167], v[14:17]
	v_mfma_f32_16x16x32_f16 v[10:13], v[180:183], v[164:167], v[10:13]
	global_load_lds_dwordx4 v[202:203], off
	v_lshl_add_u64 v[202:203], v[202:203], 0, s[22:23]
	s_add_u32 m0, s20, 0xc000
	v_mfma_f32_16x16x32_f16 v[6:9], v[184:187], v[164:167], v[6:9]
	v_mfma_f32_16x16x32_f16 v[2:5], v[188:191], v[164:167], v[2:5]
	global_load_lds_dwordx4 v[204:205], off
	v_lshl_add_u64 v[204:205], v[204:205], 0, s[22:23]
	s_add_u32 s0, s0, 0x80
	s_addc_u32 s1, s1, 0
	s_cmpk_eq_i32 s0, 0x700
	s_cbranch_scc0 .LBB2_3
	s_add_i32 s0, s15, 0
	v_add3_u32 v0, s0, v147, v148
	s_waitcnt lgkmcnt(0)
	v_mfma_f32_16x16x32_f16 v[134:137], v[98:101], v[118:121], v[134:137]
	s_add_i32 s1, s14, 1
	s_cmp_lg_u32 s1, 2
	s_cselect_b32 s1, s1, 0
	v_mfma_f32_16x16x32_f16 v[130:133], v[90:93], v[118:121], v[130:133]
	v_mfma_f32_16x16x32_f16 v[126:129], v[82:85], v[118:121], v[126:129]
	v_mfma_f32_16x16x32_f16 v[102:105], v[98:101], v[106:109], v[102:105]
	v_mfma_f32_16x16x32_f16 v[94:97], v[90:93], v[106:109], v[94:97]
	v_mfma_f32_16x16x32_f16 v[78:81], v[82:85], v[106:109], v[78:81]
	v_mfma_f32_16x16x32_f16 v[54:57], v[98:101], v[86:89], v[54:57]
	v_mfma_f32_16x16x32_f16 v[46:49], v[90:93], v[86:89], v[46:49]
	v_mfma_f32_16x16x32_f16 v[42:45], v[82:85], v[86:89], v[42:45]
	v_mfma_f32_16x16x32_f16 v[38:41], v[74:77], v[86:89], v[38:41]
	v_mfma_f32_16x16x32_f16 v[30:33], v[66:69], v[86:89], v[30:33]
	v_mfma_f32_16x16x32_f16 v[26:29], v[50:53], v[86:89], v[26:29]
	v_mfma_f32_16x16x32_f16 v[22:25], v[98:101], v[34:37], v[22:25]
	v_mfma_f32_16x16x32_f16 v[18:21], v[90:93], v[34:37], v[18:21]
	ds_read_b128 v[86:89], v0
	ds_read_b128 v[90:93], v0 offset:2048
	v_mfma_f32_16x16x32_f16 v[14:17], v[82:85], v[34:37], v[14:17]
	ds_read_b128 v[82:85], v0 offset:4096
	ds_read_b128 v[98:101], v0 offset:6144
	v_add3_u32 v0, s0, v146, v148
	v_mfma_f32_16x16x32_f16 v[122:125], v[74:77], v[118:121], v[122:125]
	v_mfma_f32_16x16x32_f16 v[114:117], v[66:69], v[118:121], v[114:117]
	v_mfma_f32_16x16x32_f16 v[110:113], v[50:53], v[118:121], v[110:113]
	v_mfma_f32_16x16x32_f16 v[70:73], v[74:77], v[106:109], v[70:73]
	v_mfma_f32_16x16x32_f16 v[62:65], v[66:69], v[106:109], v[62:65]
	v_mfma_f32_16x16x32_f16 v[58:61], v[50:53], v[106:109], v[58:61]
	v_mfma_f32_16x16x32_f16 v[10:13], v[74:77], v[34:37], v[10:13]
	ds_read_b128 v[74:77], v0 offset:32768
	ds_read_b128 v[106:109], v0 offset:34816
	v_mfma_f32_16x16x32_f16 v[6:9], v[66:69], v[34:37], v[6:9]
	ds_read_b128 v[66:69], v0 offset:36864
	ds_read_b128 v[118:121], v0 offset:38912
	ds_read_b128 v[152:155], v0 offset:40960
	ds_read_b128 v[156:159], v0 offset:43008
	v_mfma_f32_16x16x32_f16 v[0:3], v[50:53], v[34:37], v[2:5]
	s_mul_i32 s1, s1, 0xe000
	s_waitcnt vmcnt(0) lgkmcnt(0)
	s_barrier
	v_add_u32_e32 v4, s1, v150
	ds_read_b128 v[34:37], v4
	ds_read_b128 v[50:53], v4 offset:2048
	ds_read_b128 v[160:163], v4 offset:4096
	ds_read_b128 v[164:167], v4 offset:6144
	v_add_u32_e32 v4, s1, v151
	ds_read_b128 v[168:171], v4 offset:32768
	ds_read_b128 v[172:175], v4 offset:34816
	ds_read_b128 v[176:179], v4 offset:36864
	ds_read_b128 v[180:183], v4 offset:38912
	ds_read_b128 v[184:187], v4 offset:40960
	ds_read_b128 v[188:191], v4 offset:43008
	v_mfma_f32_16x16x32_f16 v[134:137], v[74:77], v[86:89], v[134:137]
	v_mfma_f32_16x16x32_f16 v[130:133], v[106:109], v[86:89], v[130:133]
	v_mfma_f32_16x16x32_f16 v[126:129], v[66:69], v[86:89], v[126:129]
	v_mfma_f32_16x16x32_f16 v[122:125], v[118:121], v[86:89], v[122:125]
	v_mfma_f32_16x16x32_f16 v[114:117], v[152:155], v[86:89], v[114:117]
	v_mfma_f32_16x16x32_f16 v[86:89], v[156:159], v[86:89], v[110:113]
	v_mfma_f32_16x16x32_f16 v[102:105], v[74:77], v[90:93], v[102:105]
	v_mfma_f32_16x16x32_f16 v[94:97], v[106:109], v[90:93], v[94:97]
	v_mfma_f32_16x16x32_f16 v[78:81], v[66:69], v[90:93], v[78:81]
	v_mfma_f32_16x16x32_f16 v[70:73], v[118:121], v[90:93], v[70:73]
	v_mfma_f32_16x16x32_f16 v[62:65], v[152:155], v[90:93], v[62:65]
	v_mfma_f32_16x16x32_f16 v[58:61], v[156:159], v[90:93], v[58:61]
	v_mfma_f32_16x16x32_f16 v[54:57], v[74:77], v[82:85], v[54:57]
	v_mfma_f32_16x16x32_f16 v[46:49], v[106:109], v[82:85], v[46:49]
	v_mfma_f32_16x16x32_f16 v[42:45], v[66:69], v[82:85], v[42:45]
	v_mfma_f32_16x16x32_f16 v[38:41], v[118:121], v[82:85], v[38:41]
	v_mfma_f32_16x16x32_f16 v[30:33], v[152:155], v[82:85], v[30:33]
	v_mfma_f32_16x16x32_f16 v[26:29], v[156:159], v[82:85], v[26:29]
	v_mfma_f32_16x16x32_f16 v[22:25], v[74:77], v[98:101], v[22:25]
	v_mfma_f32_16x16x32_f16 v[18:21], v[106:109], v[98:101], v[18:21]
	v_mfma_f32_16x16x32_f16 v[14:17], v[66:69], v[98:101], v[14:17]
	v_mfma_f32_16x16x32_f16 v[10:13], v[118:121], v[98:101], v[10:13]
	v_mfma_f32_16x16x32_f16 v[4:7], v[152:155], v[98:101], v[6:9]
	v_mfma_f32_16x16x32_f16 v[0:3], v[156:159], v[98:101], v[0:3]
	s_add_i32 s0, s1, 0
	s_nop 0
	v_add3_u32 v8, s0, v147, v148
	s_waitcnt lgkmcnt(5)
	v_mfma_f32_16x16x32_f16 v[66:69], v[168:171], v[34:37], v[134:137]
	s_waitcnt lgkmcnt(4)
	v_mfma_f32_16x16x32_f16 v[74:77], v[172:175], v[34:37], v[130:133]
	s_waitcnt lgkmcnt(3)
	v_mfma_f32_16x16x32_f16 v[82:85], v[176:179], v[34:37], v[126:129]
	s_waitcnt lgkmcnt(2)
	v_mfma_f32_16x16x32_f16 v[90:93], v[180:183], v[34:37], v[122:125]
	s_waitcnt lgkmcnt(1)
	v_mfma_f32_16x16x32_f16 v[98:101], v[184:187], v[34:37], v[114:117]
	s_waitcnt lgkmcnt(0)
	v_mfma_f32_16x16x32_f16 v[34:37], v[188:191], v[34:37], v[86:89]
	v_mfma_f32_16x16x32_f16 v[86:89], v[168:171], v[50:53], v[102:105]
	v_mfma_f32_16x16x32_f16 v[94:97], v[172:175], v[50:53], v[94:97]
	v_mfma_f32_16x16x32_f16 v[78:81], v[176:179], v[50:53], v[78:81]
	v_mfma_f32_16x16x32_f16 v[70:73], v[180:183], v[50:53], v[70:73]
	v_mfma_f32_16x16x32_f16 v[62:65], v[184:187], v[50:53], v[62:65]
	v_mfma_f32_16x16x32_f16 v[50:53], v[188:191], v[50:53], v[58:61]
	s_nop 2
	ds_read_b128 v[58:61], v8
	ds_read_b128 v[102:105], v8 offset:2048
	ds_read_b128 v[106:109], v8 offset:4096
	ds_read_b128 v[110:113], v8 offset:6144
	v_mfma_f32_16x16x32_f16 v[8:11], v[180:183], v[164:167], v[10:13]
	s_nop 2
	v_add3_u32 v12, s0, v146, v148
	ds_read_b128 v[114:117], v12 offset:32768
	ds_read_b128 v[118:121], v12 offset:34816
	ds_read_b128 v[122:125], v12 offset:36864
	ds_read_b128 v[126:129], v12 offset:38912
	ds_read_b128 v[130:133], v12 offset:40960
	ds_read_b128 v[134:137], v12 offset:43008
	v_mfma_f32_16x16x32_f16 v[54:57], v[168:171], v[160:163], v[54:57]
	v_mfma_f32_16x16x32_f16 v[46:49], v[172:175], v[160:163], v[46:49]
	v_mfma_f32_16x16x32_f16 v[42:45], v[176:179], v[160:163], v[42:45]
	v_mfma_f32_16x16x32_f16 v[38:41], v[180:183], v[160:163], v[38:41]
	v_mfma_f32_16x16x32_f16 v[30:33], v[184:187], v[160:163], v[30:33]
	v_mfma_f32_16x16x32_f16 v[26:29], v[188:191], v[160:163], v[26:29]
	v_mfma_f32_16x16x32_f16 v[22:25], v[168:171], v[164:167], v[22:25]
	v_mfma_f32_16x16x32_f16 v[18:21], v[172:175], v[164:167], v[18:21]
	v_mfma_f32_16x16x32_f16 v[14:17], v[176:179], v[164:167], v[14:17]
	v_mfma_f32_16x16x32_f16 v[4:7], v[184:187], v[164:167], v[4:7]
	v_mfma_f32_16x16x32_f16 v[0:3], v[188:191], v[164:167], v[0:3]
	s_waitcnt vmcnt(0) lgkmcnt(0)
	s_barrier
	v_mfma_f32_16x16x32_f16 v[66:69], v[114:117], v[58:61], v[66:69]
	v_mfma_f32_16x16x32_f16 v[74:77], v[118:121], v[58:61], v[74:77]
	v_mfma_f32_16x16x32_f16 v[82:85], v[122:125], v[58:61], v[82:85]
	v_mfma_f32_16x16x32_f16 v[90:93], v[126:129], v[58:61], v[90:93]
	v_mfma_f32_16x16x32_f16 v[98:101], v[130:133], v[58:61], v[98:101]
	v_mfma_f32_16x16x32_f16 v[34:37], v[134:137], v[58:61], v[34:37]
	v_mfma_f32_16x16x32_f16 v[58:61], v[114:117], v[102:105], v[86:89]
	v_mfma_f32_16x16x32_f16 v[86:89], v[118:121], v[102:105], v[94:97]
	v_mfma_f32_16x16x32_f16 v[78:81], v[122:125], v[102:105], v[78:81]
	v_mfma_f32_16x16x32_f16 v[70:73], v[126:129], v[102:105], v[70:73]
	v_mfma_f32_16x16x32_f16 v[62:65], v[130:133], v[102:105], v[62:65]
	v_mfma_f32_16x16x32_f16 v[50:53], v[134:137], v[102:105], v[50:53]
	v_mfma_f32_16x16x32_f16 v[54:57], v[114:117], v[106:109], v[54:57]
	v_mfma_f32_16x16x32_f16 v[46:49], v[118:121], v[106:109], v[46:49]
	v_mfma_f32_16x16x32_f16 v[42:45], v[122:125], v[106:109], v[42:45]
	v_mfma_f32_16x16x32_f16 v[38:41], v[126:129], v[106:109], v[38:41]
	v_mfma_f32_16x16x32_f16 v[30:33], v[130:133], v[106:109], v[30:33]
	v_mfma_f32_16x16x32_f16 v[26:29], v[134:137], v[106:109], v[26:29]
	v_mfma_f32_16x16x32_f16 v[22:25], v[114:117], v[110:113], v[22:25]
	v_mfma_f32_16x16x32_f16 v[18:21], v[118:121], v[110:113], v[18:21]
	v_mfma_f32_16x16x32_f16 v[12:15], v[122:125], v[110:113], v[14:17]
	v_mfma_f32_16x16x32_f16 v[8:11], v[126:129], v[110:113], v[8:11]
	v_mfma_f32_16x16x32_f16 v[4:7], v[130:133], v[110:113], v[4:7]
	v_mfma_f32_16x16x32_f16 v[0:3], v[134:137], v[110:113], v[0:3]
	s_movk_i32 s0, 0x3400
	v_mad_u32_u24 v94, v144, s0, 0
	v_lshlrev_b32_e32 v16, 3, v145
	v_mul_u32_u24_e32 v17, 0xd0, v143
	v_add3_u32 v95, v94, v16, v17
	v_cvt_pk_f16_f32 v17, v68, v69
	v_cvt_pk_f16_f32 v16, v66, v67
	v_cvt_pk_f16_f32 v67, v76, v77
	v_cvt_pk_f16_f32 v66, v74, v75
	s_barrier
	ds_write2_b64 v95, v[16:17], v[66:67] offset1:4
	v_cvt_pk_f16_f32 v17, v84, v85
	v_cvt_pk_f16_f32 v16, v82, v83
	v_cvt_pk_f16_f32 v67, v92, v93
	v_cvt_pk_f16_f32 v66, v90, v91
	s_mov_b32 s0, 0x15555556
	ds_write2_b64 v95, v[16:17], v[66:67] offset0:8 offset1:12
	v_cvt_pk_f16_f32 v17, v100, v101
	v_cvt_pk_f16_f32 v16, v98, v99
	v_cvt_pk_f16_f32 v37, v36, v37
	v_cvt_pk_f16_f32 v36, v34, v35
	v_cvt_pk_f16_f32 v7, v6, v7
	v_cvt_pk_f16_f32 v6, v4, v5
	v_mul_hi_u32 v4, v140, s0
	ds_write2_b64 v95, v[16:17], v[36:37] offset0:16 offset1:20
	v_cvt_pk_f16_f32 v17, v60, v61
	v_cvt_pk_f16_f32 v16, v58, v59
	v_cvt_pk_f16_f32 v35, v88, v89
	v_cvt_pk_f16_f32 v34, v86, v87
	v_add_u32_e32 v36, 0x800, v95
	v_cvt_pk_f16_f32 v21, v20, v21
	v_cvt_pk_f16_f32 v20, v18, v19
	v_add_u32_e32 v18, 0x2000, v95
	v_cvt_pk_f16_f32 v15, v14, v15
	v_cvt_pk_f16_f32 v14, v12, v13
	v_cvt_pk_f16_f32 v11, v10, v11
	v_cvt_pk_f16_f32 v10, v8, v9
	v_cvt_pk_f16_f32 v3, v2, v3
	v_cvt_pk_f16_f32 v2, v0, v1
	v_mul_u32_u24_e32 v0, 12, v4
	ds_write2_b64 v36, v[16:17], v[34:35] offset0:160 offset1:164
	v_cvt_pk_f16_f32 v17, v80, v81
	v_cvt_pk_f16_f32 v16, v78, v79
	v_cvt_pk_f16_f32 v35, v72, v73
	v_cvt_pk_f16_f32 v34, v70, v71
	ds_write2_b64 v18, v[14:15], v[10:11] offset0:232 offset1:236
	v_add_u32_e32 v10, s13, v142
	v_sub_u32_e32 v5, v140, v0
	ds_write2_b64 v36, v[16:17], v[34:35] offset0:168 offset1:172
	v_cvt_pk_f16_f32 v17, v64, v65
	v_cvt_pk_f16_f32 v16, v62, v63
	v_cvt_pk_f16_f32 v35, v52, v53
	v_cvt_pk_f16_f32 v34, v50, v51
	v_lshl_add_u32 v12, v5, 3, v10
	ds_write2_b64 v36, v[16:17], v[34:35] offset0:176 offset1:180
	v_cvt_pk_f16_f32 v17, v56, v57
	v_cvt_pk_f16_f32 v16, v54, v55
	v_cvt_pk_f16_f32 v35, v48, v49
	v_cvt_pk_f16_f32 v34, v46, v47
	v_add_u32_e32 v36, 0x1800, v95
	v_lshrrev_b32_e32 v0, 10, v12
	v_mov_b32_e32 v1, 0
	ds_write2_b64 v36, v[16:17], v[34:35] offset0:64 offset1:68
	v_cvt_pk_f16_f32 v17, v44, v45
	v_cvt_pk_f16_f32 v16, v42, v43
	v_cvt_pk_f16_f32 v35, v40, v41
	v_cvt_pk_f16_f32 v34, v38, v39
	ds_write2_b64 v18, v[6:7], v[2:3] offset0:240 offset1:244
	v_add_u32_e32 v11, s12, v141
	v_lshlrev_b64 v[2:3], 23, v[0:1]
	ds_write2_b64 v36, v[16:17], v[34:35] offset0:72 offset1:76
	v_cvt_pk_f16_f32 v17, v32, v33
	v_cvt_pk_f16_f32 v16, v30, v31
	v_cvt_pk_f16_f32 v29, v28, v29
	v_cvt_pk_f16_f32 v28, v26, v27
	v_lshl_add_u64 v[6:7], s[8:9], 0, v[2:3]
	v_or_b32_e32 v2, v11, v4
	ds_write2_b64 v36, v[16:17], v[28:29] offset0:80 offset1:84
	v_cvt_pk_f16_f32 v17, v24, v25
	v_cvt_pk_f16_f32 v16, v22, v23
	v_ashrrev_i32_e32 v3, 31, v2
	ds_write2_b64 v18, v[16:17], v[20:21] offset0:224 offset1:228
	v_lshlrev_b64 v[8:9], 11, v[2:3]
	v_mul_u32_u24_e32 v0, 0xd0, v4
	v_lshlrev_b32_e32 v2, 4, v5
	s_waitcnt lgkmcnt(0)
	v_add3_u32 v0, v94, v0, v2
	ds_read_b128 v[2:5], v0
	v_and_b32_e32 v0, 0x3f8, v12
	v_lshl_add_u64 v[6:7], v[6:7], 0, v[8:9]
	v_lshlrev_b32_e32 v0, 1, v0
	v_lshl_add_u64 v[6:7], v[6:7], 0, v[0:1]
	v_or_b32_e32 v0, 64, v140
	s_waitcnt lgkmcnt(0)
	global_store_dwordx4 v[6:7], v[2:5], off sc1
	s_nop 1
	v_mul_hi_u32 v4, v0, s0
	v_mul_u32_u24_e32 v2, 12, v4
	v_sub_u32_e32 v5, v0, v2
	v_lshl_add_u32 v12, v5, 3, v10
	v_lshrrev_b32_e32 v0, 10, v12
	v_lshlrev_b64 v[2:3], 23, v[0:1]
	v_lshl_add_u64 v[6:7], s[8:9], 0, v[2:3]
	v_or_b32_e32 v2, v11, v4
	v_ashrrev_i32_e32 v3, 31, v2
	v_lshlrev_b64 v[8:9], 11, v[2:3]
	v_mul_u32_u24_e32 v0, 0xd0, v4
	v_lshlrev_b32_e32 v2, 4, v5
	v_add3_u32 v0, v94, v0, v2
	ds_read_b128 v[2:5], v0
	v_and_b32_e32 v0, 0x3f8, v12
	v_lshl_add_u64 v[6:7], v[6:7], 0, v[8:9]
	v_lshlrev_b32_e32 v0, 1, v0
	v_lshl_add_u64 v[6:7], v[6:7], 0, v[0:1]
	v_or_b32_e32 v0, 0x80, v140
	s_waitcnt lgkmcnt(0)
	global_store_dwordx4 v[6:7], v[2:5], off sc1
	s_nop 1
	v_mul_hi_u32 v4, v0, s0
	v_mul_u32_u24_e32 v2, 12, v4
	v_sub_u32_e32 v5, v0, v2
	v_lshl_add_u32 v12, v5, 3, v10
	v_lshrrev_b32_e32 v0, 10, v12
	v_lshlrev_b64 v[2:3], 23, v[0:1]
	v_lshl_add_u64 v[6:7], s[8:9], 0, v[2:3]
	v_or_b32_e32 v2, v11, v4
	v_ashrrev_i32_e32 v3, 31, v2
	v_lshlrev_b64 v[8:9], 11, v[2:3]
	v_mul_u32_u24_e32 v0, 0xd0, v4
	v_lshlrev_b32_e32 v2, 4, v5
	v_add3_u32 v0, v94, v0, v2
	ds_read_b128 v[2:5], v0
	v_and_b32_e32 v0, 0x3f8, v12
	v_lshl_add_u64 v[6:7], v[6:7], 0, v[8:9]
	v_lshlrev_b32_e32 v0, 1, v0
	v_lshl_add_u64 v[6:7], v[6:7], 0, v[0:1]
	v_or_b32_e32 v0, 0xc0, v140
	s_waitcnt lgkmcnt(0)
	global_store_dwordx4 v[6:7], v[2:5], off sc1
	s_nop 1
	v_mul_hi_u32 v4, v0, s0
	v_mul_u32_u24_e32 v2, 12, v4
	v_sub_u32_e32 v5, v0, v2
	v_lshl_add_u32 v12, v5, 3, v10
	v_lshrrev_b32_e32 v0, 10, v12
	v_lshlrev_b64 v[2:3], 23, v[0:1]
	v_lshl_add_u64 v[6:7], s[8:9], 0, v[2:3]
	v_or_b32_e32 v2, v11, v4
	v_ashrrev_i32_e32 v3, 31, v2
	v_lshlrev_b64 v[8:9], 11, v[2:3]
	v_mul_u32_u24_e32 v0, 0xd0, v4
	v_lshlrev_b32_e32 v2, 4, v5
	v_add3_u32 v0, v94, v0, v2
	ds_read_b128 v[2:5], v0
	v_and_b32_e32 v0, 0x3f8, v12
	v_lshl_add_u64 v[6:7], v[6:7], 0, v[8:9]
	v_lshlrev_b32_e32 v0, 1, v0
	v_lshl_add_u64 v[6:7], v[6:7], 0, v[0:1]
	v_or_b32_e32 v0, 0x100, v140
	s_waitcnt lgkmcnt(0)
	global_store_dwordx4 v[6:7], v[2:5], off sc1
	s_nop 1
	v_mul_hi_u32 v4, v0, s0
	v_mul_u32_u24_e32 v2, 12, v4
	v_sub_u32_e32 v5, v0, v2
	v_lshl_add_u32 v12, v5, 3, v10
	v_lshrrev_b32_e32 v0, 10, v12
	v_lshlrev_b64 v[2:3], 23, v[0:1]
	v_lshl_add_u64 v[6:7], s[8:9], 0, v[2:3]
	v_or_b32_e32 v2, v11, v4
	v_ashrrev_i32_e32 v3, 31, v2
	v_lshlrev_b64 v[8:9], 11, v[2:3]
	v_mul_u32_u24_e32 v0, 0xd0, v4
	v_lshlrev_b32_e32 v2, 4, v5
	v_add3_u32 v0, v94, v0, v2
	ds_read_b128 v[2:5], v0
	v_and_b32_e32 v0, 0x3f8, v12
	v_lshl_add_u64 v[6:7], v[6:7], 0, v[8:9]
	v_lshlrev_b32_e32 v0, 1, v0
	v_lshl_add_u64 v[6:7], v[6:7], 0, v[0:1]
	v_or_b32_e32 v0, 0x140, v140
	s_waitcnt lgkmcnt(0)
	global_store_dwordx4 v[6:7], v[2:5], off sc1
	s_nop 1
	v_mul_hi_u32 v4, v0, s0
	v_mul_u32_u24_e32 v2, 12, v4
	v_sub_u32_e32 v5, v0, v2
	v_lshl_add_u32 v12, v5, 3, v10
	v_lshrrev_b32_e32 v0, 10, v12
	v_lshlrev_b64 v[2:3], 23, v[0:1]
	v_lshl_add_u64 v[6:7], s[8:9], 0, v[2:3]
	v_or_b32_e32 v2, v11, v4
	v_ashrrev_i32_e32 v3, 31, v2
	v_lshlrev_b64 v[8:9], 11, v[2:3]
	v_mul_u32_u24_e32 v0, 0xd0, v4
	v_lshlrev_b32_e32 v2, 4, v5
	v_add3_u32 v0, v94, v0, v2
	ds_read_b128 v[2:5], v0
	v_and_b32_e32 v0, 0x3f8, v12
	v_lshl_add_u64 v[6:7], v[6:7], 0, v[8:9]
	v_lshlrev_b32_e32 v0, 1, v0
	v_lshl_add_u64 v[6:7], v[6:7], 0, v[0:1]
	v_or_b32_e32 v0, 0x180, v140
	s_waitcnt lgkmcnt(0)
	global_store_dwordx4 v[6:7], v[2:5], off sc1
	s_nop 1
	v_mul_hi_u32 v4, v0, s0
	v_mul_u32_u24_e32 v2, 12, v4
	v_sub_u32_e32 v5, v0, v2
	v_lshl_add_u32 v12, v5, 3, v10
	v_lshrrev_b32_e32 v0, 10, v12
	v_lshlrev_b64 v[2:3], 23, v[0:1]
	v_lshl_add_u64 v[6:7], s[8:9], 0, v[2:3]
	v_or_b32_e32 v2, v11, v4
	v_ashrrev_i32_e32 v3, 31, v2
	v_lshlrev_b64 v[8:9], 11, v[2:3]
	v_mul_u32_u24_e32 v0, 0xd0, v4
	v_lshlrev_b32_e32 v2, 4, v5
	v_add3_u32 v0, v94, v0, v2
	ds_read_b128 v[2:5], v0
	v_and_b32_e32 v0, 0x3f8, v12
	v_lshl_add_u64 v[6:7], v[6:7], 0, v[8:9]
	v_lshlrev_b32_e32 v0, 1, v0
	v_lshl_add_u64 v[6:7], v[6:7], 0, v[0:1]
	v_or_b32_e32 v0, 0x1c0, v140
	s_waitcnt lgkmcnt(0)
	global_store_dwordx4 v[6:7], v[2:5], off sc1
	s_nop 1
	v_mul_hi_u32 v4, v0, s0
	v_mul_u32_u24_e32 v2, 12, v4
	v_sub_u32_e32 v5, v0, v2
	v_lshl_add_u32 v12, v5, 3, v10
	v_lshrrev_b32_e32 v0, 10, v12
	v_lshlrev_b64 v[2:3], 23, v[0:1]
	v_lshl_add_u64 v[6:7], s[8:9], 0, v[2:3]
	v_or_b32_e32 v2, v11, v4
	v_ashrrev_i32_e32 v3, 31, v2
	v_lshlrev_b64 v[8:9], 11, v[2:3]
	v_mul_u32_u24_e32 v0, 0xd0, v4
	v_lshlrev_b32_e32 v2, 4, v5
	v_add3_u32 v0, v94, v0, v2
	ds_read_b128 v[2:5], v0
	v_and_b32_e32 v0, 0x3f8, v12
	v_lshl_add_u64 v[6:7], v[6:7], 0, v[8:9]
	v_lshlrev_b32_e32 v0, 1, v0
	v_lshl_add_u64 v[6:7], v[6:7], 0, v[0:1]
	v_or_b32_e32 v0, 0x200, v140
	s_waitcnt lgkmcnt(0)
	global_store_dwordx4 v[6:7], v[2:5], off sc1
	s_nop 1
	v_mul_hi_u32 v4, v0, s0
	v_mul_u32_u24_e32 v2, 12, v4
	v_sub_u32_e32 v5, v0, v2
	v_lshl_add_u32 v12, v5, 3, v10
	v_lshrrev_b32_e32 v0, 10, v12
	v_lshlrev_b64 v[2:3], 23, v[0:1]
	v_lshl_add_u64 v[6:7], s[8:9], 0, v[2:3]
	v_or_b32_e32 v2, v11, v4
	v_ashrrev_i32_e32 v3, 31, v2
	v_lshlrev_b64 v[8:9], 11, v[2:3]
	v_mul_u32_u24_e32 v0, 0xd0, v4
	v_lshlrev_b32_e32 v2, 4, v5
	v_add3_u32 v0, v94, v0, v2
	ds_read_b128 v[2:5], v0
	v_and_b32_e32 v0, 0x3f8, v12
	v_lshl_add_u64 v[6:7], v[6:7], 0, v[8:9]
	v_lshlrev_b32_e32 v0, 1, v0
	v_lshl_add_u64 v[6:7], v[6:7], 0, v[0:1]
	v_or_b32_e32 v0, 0x240, v140
	s_waitcnt lgkmcnt(0)
	global_store_dwordx4 v[6:7], v[2:5], off sc1
	s_nop 1
	v_mul_hi_u32 v4, v0, s0
	v_mul_u32_u24_e32 v2, 12, v4
	v_sub_u32_e32 v5, v0, v2
	v_lshl_add_u32 v12, v5, 3, v10
	v_lshrrev_b32_e32 v0, 10, v12
	v_lshlrev_b64 v[2:3], 23, v[0:1]
	v_lshl_add_u64 v[6:7], s[8:9], 0, v[2:3]
	v_or_b32_e32 v2, v11, v4
	v_ashrrev_i32_e32 v3, 31, v2
	v_lshlrev_b64 v[8:9], 11, v[2:3]
	v_mul_u32_u24_e32 v0, 0xd0, v4
	v_lshlrev_b32_e32 v2, 4, v5
	v_add3_u32 v0, v94, v0, v2
	ds_read_b128 v[2:5], v0
	v_and_b32_e32 v0, 0x3f8, v12
	v_lshl_add_u64 v[6:7], v[6:7], 0, v[8:9]
	v_lshlrev_b32_e32 v0, 1, v0
	v_lshl_add_u64 v[6:7], v[6:7], 0, v[0:1]
	v_or_b32_e32 v0, 0x280, v140
	s_waitcnt lgkmcnt(0)
	global_store_dwordx4 v[6:7], v[2:5], off sc1
	s_nop 1
	v_mul_hi_u32 v4, v0, s0
	v_mul_u32_u24_e32 v2, 12, v4
	v_sub_u32_e32 v5, v0, v2
	v_lshl_add_u32 v12, v5, 3, v10
	v_lshrrev_b32_e32 v0, 10, v12
	v_lshlrev_b64 v[2:3], 23, v[0:1]
	v_lshl_add_u64 v[6:7], s[8:9], 0, v[2:3]
	v_or_b32_e32 v2, v11, v4
	v_ashrrev_i32_e32 v3, 31, v2
	v_lshlrev_b64 v[8:9], 11, v[2:3]
	v_mul_u32_u24_e32 v0, 0xd0, v4
	v_lshlrev_b32_e32 v2, 4, v5
	v_add3_u32 v0, v94, v0, v2
	ds_read_b128 v[2:5], v0
	v_and_b32_e32 v0, 0x3f8, v12
	v_lshl_add_u64 v[6:7], v[6:7], 0, v[8:9]
	v_lshlrev_b32_e32 v0, 1, v0
	v_lshl_add_u64 v[6:7], v[6:7], 0, v[0:1]
	v_or_b32_e32 v0, 0x2c0, v140
	s_waitcnt lgkmcnt(0)
	global_store_dwordx4 v[6:7], v[2:5], off sc1
	s_nop 1
	v_mul_hi_u32 v4, v0, s0
	v_mul_u32_u24_e32 v2, 12, v4
	v_sub_u32_e32 v5, v0, v2
	v_lshl_add_u32 v10, v5, 3, v10
	v_lshrrev_b32_e32 v0, 10, v10
	v_lshlrev_b64 v[2:3], 23, v[0:1]
	v_lshl_add_u64 v[6:7], s[8:9], 0, v[2:3]
	v_or_b32_e32 v2, v11, v4
	v_ashrrev_i32_e32 v3, 31, v2
	v_lshlrev_b64 v[8:9], 11, v[2:3]
	v_mul_u32_u24_e32 v0, 0xd0, v4
	v_lshlrev_b32_e32 v2, 4, v5
	v_add3_u32 v0, v94, v0, v2
	ds_read_b128 v[2:5], v0
	v_and_b32_e32 v0, 0x3f8, v10
	v_lshl_add_u64 v[6:7], v[6:7], 0, v[8:9]
	v_lshlrev_b32_e32 v0, 1, v0
	v_lshl_add_u64 v[0:1], v[6:7], 0, v[0:1]
	s_waitcnt lgkmcnt(0)
	global_store_dwordx4 v[0:1], v[2:5], off sc1
	s_nop 1
	s_endpgm
	s_nop 0
	s_nop 0
	s_nop 0
	s_nop 0
	s_nop 0
	s_nop 0
	s_nop 0
	s_nop 0
	s_nop 0
	s_nop 0
	s_nop 0
	s_nop 0
	s_nop 0
	s_nop 0
	s_nop 0
	s_nop 0
	s_nop 0
	s_nop 0
	s_nop 0
	s_nop 0
	s_nop 0
	s_nop 0
	s_nop 0
	s_nop 0
	s_nop 0
	s_nop 0
	s_nop 0
	s_nop 0
	s_nop 0
	s_nop 0
	s_nop 0
	s_nop 0
	s_nop 0
	s_nop 0
	s_nop 0
	s_nop 0
	s_nop 0
	s_nop 0
	s_nop 0
	s_nop 0
	s_nop 0
	s_nop 0
	s_nop 0
	s_nop 0
	s_nop 0
	s_nop 0
	s_nop 0
	s_nop 0
	s_endpgm
